# GEMM K-loops (all four): LDS-DMA loads use scalar base + 32-bit VGPR offset (saddr) instead of 64-bit VGPR addresses; 16 v_lshl_add_u64 per trip removed from the load segments
# speedup vs baseline: 1.0067x; 1.0067x over previous
.LBB0_191:
	s_add_u32 s42, s40, 0xfff80080
	s_addc_u32 s43, s41, -1
	s_add_i32 s91, 0, 0x10000
	s_cmp_eq_u32 s90, 28
	s_cselect_b32 s45, s9, s43
	s_cselect_b32 s44, s86, s42
	s_cselect_b32 s43, s11, s89
	s_cselect_b32 s42, s87, s88
	s_add_i32 s94, 0, 0x14000
	v_add_u32_e32 v160, s91, v154
	v_add_u32_e32 v176, s94, v154
	ds_read_b128 v[146:149], v160
	ds_read_b128 v[150:153], v160 offset:1024
	ds_read_b128 v[156:159], v160 offset:2048
	ds_read_b128 v[160:163], v160 offset:3072
	ds_read_b128 v[164:167], v176
	ds_read_b128 v[168:171], v176 offset:1024
	ds_read_b128 v[172:175], v176 offset:2048
	ds_read_b128 v[176:179], v176 offset:3072
	s_add_i32 m0, s60, 0xc000
	ds_read_b128 v[180:183], v155
	ds_read_b128 v[184:187], v155 offset:1024
	ds_read_b128 v[188:191], v155 offset:2048
	ds_read_b128 v[192:195], v155 offset:3072
	ds_read_b128 v[196:199], v155 offset:4096
	ds_read_b128 v[200:203], v155 offset:5120
	ds_read_b128 v[204:207], v155 offset:6144
	ds_read_b128 v[218:221], v155 offset:7168
	global_load_lds_dwordx4 v142, s[40:41]
	s_add_i32 m0, s60, 0xe000
	s_nop 0
	global_load_lds_dwordx4 v144, s[40:41]
	s_waitcnt vmcnt(8)
	s_waitcnt lgkmcnt(0)
	s_barrier
	s_setprio 1
	s_waitcnt lgkmcnt(0)
	v_mfma_f32_16x16x32_bf16 v[128:131], v[146:149], v[180:183], v[128:131]
	v_mfma_f32_16x16x32_bf16 v[124:127], v[156:159], v[180:183], v[124:127]
	v_mfma_f32_16x16x32_bf16 v[120:123], v[146:149], v[188:191], v[120:123]
	v_mfma_f32_16x16x32_bf16 v[116:119], v[156:159], v[188:191], v[116:119]
	v_mfma_f32_16x16x32_bf16 v[112:115], v[146:149], v[196:199], v[112:115]
	v_mfma_f32_16x16x32_bf16 v[104:107], v[156:159], v[196:199], v[104:107]
	v_mfma_f32_16x16x32_bf16 v[96:99], v[146:149], v[204:207], v[96:99]
	v_mfma_f32_16x16x32_bf16 v[88:91], v[156:159], v[204:207], v[88:91]
	v_mfma_f32_16x16x32_bf16 v[128:131], v[150:153], v[184:187], v[128:131]
	v_mfma_f32_16x16x32_bf16 v[124:127], v[160:163], v[184:187], v[124:127]
	v_mfma_f32_16x16x32_bf16 v[120:123], v[150:153], v[192:195], v[120:123]
	v_mfma_f32_16x16x32_bf16 v[116:119], v[160:163], v[192:195], v[116:119]
	v_mfma_f32_16x16x32_bf16 v[112:115], v[150:153], v[200:203], v[112:115]
	v_mfma_f32_16x16x32_bf16 v[104:107], v[160:163], v[200:203], v[104:107]
	v_mfma_f32_16x16x32_bf16 v[96:99], v[150:153], v[218:221], v[96:99]
	v_mfma_f32_16x16x32_bf16 v[88:91], v[160:163], v[218:221], v[88:91]
	s_setprio 0
	s_setprio 1
	v_mfma_f32_16x16x32_bf16 v[108:111], v[164:167], v[180:183], v[108:111]
	v_mfma_f32_16x16x32_bf16 v[100:103], v[172:175], v[180:183], v[100:103]
	v_mfma_f32_16x16x32_bf16 v[92:95], v[164:167], v[188:191], v[92:95]
	v_mfma_f32_16x16x32_bf16 v[84:87], v[172:175], v[188:191], v[84:87]
	v_mfma_f32_16x16x32_bf16 v[80:83], v[164:167], v[196:199], v[80:83]
	v_mfma_f32_16x16x32_bf16 v[76:79], v[172:175], v[196:199], v[76:79]
	v_mfma_f32_16x16x32_bf16 v[72:75], v[164:167], v[204:207], v[72:75]
	v_mfma_f32_16x16x32_bf16 v[68:71], v[172:175], v[204:207], v[68:71]
	v_mfma_f32_16x16x32_bf16 v[108:111], v[168:171], v[184:187], v[108:111]
	v_mfma_f32_16x16x32_bf16 v[100:103], v[176:179], v[184:187], v[100:103]
	v_mfma_f32_16x16x32_bf16 v[92:95], v[168:171], v[192:195], v[92:95]
	v_mfma_f32_16x16x32_bf16 v[84:87], v[176:179], v[192:195], v[84:87]
	v_mfma_f32_16x16x32_bf16 v[80:83], v[168:171], v[200:203], v[80:83]
	v_mfma_f32_16x16x32_bf16 v[76:79], v[176:179], v[200:203], v[76:79]
	v_mfma_f32_16x16x32_bf16 v[72:75], v[168:171], v[218:221], v[72:75]
	v_mfma_f32_16x16x32_bf16 v[68:71], v[176:179], v[218:221], v[68:71]
	s_setprio 0
	s_barrier
	s_add_i32 s91, s91, s51
	s_mov_b32 m0, s91
	ds_read_b128 v[180:183], v155 offset:16384
	ds_read_b128 v[184:187], v155 offset:17408
	ds_read_b128 v[188:191], v155 offset:18432
	ds_read_b128 v[192:195], v155 offset:19456
	ds_read_b128 v[196:199], v155 offset:20480
	ds_read_b128 v[200:203], v155 offset:21504
	ds_read_b128 v[204:207], v155 offset:22528
	ds_read_b128 v[218:221], v155 offset:23552
	global_load_lds_dwordx4 v2, s[42:43]
	s_add_i32 m0, s91, 0x2000
	s_add_u32 s92, s42, 0x80000
	s_addc_u32 s93, s43, 0
	s_add_i32 s91, s94, s51
	global_load_lds_dwordx4 v132, s[42:43]
	s_mov_b32 m0, s91
	s_nop 0
	global_load_lds_dwordx4 v2, s[92:93]
	s_add_i32 m0, s91, 0x2000
	s_nop 0
	global_load_lds_dwordx4 v132, s[92:93]
	s_mov_b32 m0, s60
	s_nop 0
	global_load_lds_dwordx4 v136, s[44:45]
	s_mov_b32 m0, s61
	s_nop 0
	global_load_lds_dwordx4 v134, s[44:45]
	s_add_u32 s98, s42, s16
	s_addc_u32 s99, s43, s17
	s_add_u32 vcc_lo, s44, s16
	s_addc_u32 vcc_hi, s45, s17
	s_waitcnt vmcnt(8)
	s_waitcnt lgkmcnt(0)
	s_barrier
	s_setprio 1
	s_waitcnt lgkmcnt(0)
	v_mfma_f32_16x16x32_bf16 v[64:67], v[146:149], v[180:183], v[64:67]
	v_mfma_f32_16x16x32_bf16 v[60:63], v[156:159], v[180:183], v[60:63]
	v_mfma_f32_16x16x32_bf16 v[56:59], v[146:149], v[188:191], v[56:59]
	v_mfma_f32_16x16x32_bf16 v[52:55], v[156:159], v[188:191], v[52:55]
	v_mfma_f32_16x16x32_bf16 v[40:43], v[146:149], v[196:199], v[40:43]
	v_mfma_f32_16x16x32_bf16 v[36:39], v[156:159], v[196:199], v[36:39]
	v_mfma_f32_16x16x32_bf16 v[24:27], v[146:149], v[204:207], v[24:27]
	v_mfma_f32_16x16x32_bf16 v[20:23], v[156:159], v[204:207], v[20:23]
	v_mfma_f32_16x16x32_bf16 v[64:67], v[150:153], v[184:187], v[64:67]
	v_mfma_f32_16x16x32_bf16 v[60:63], v[160:163], v[184:187], v[60:63]
	v_mfma_f32_16x16x32_bf16 v[56:59], v[150:153], v[192:195], v[56:59]
	v_mfma_f32_16x16x32_bf16 v[52:55], v[160:163], v[192:195], v[52:55]
	v_mfma_f32_16x16x32_bf16 v[40:43], v[150:153], v[200:203], v[40:43]
	v_mfma_f32_16x16x32_bf16 v[36:39], v[160:163], v[200:203], v[36:39]
	v_mfma_f32_16x16x32_bf16 v[24:27], v[150:153], v[218:221], v[24:27]
	v_mfma_f32_16x16x32_bf16 v[20:23], v[160:163], v[218:221], v[20:23]
	s_setprio 0
	s_setprio 1
	v_mfma_f32_16x16x32_bf16 v[48:51], v[164:167], v[180:183], v[48:51]
	v_mfma_f32_16x16x32_bf16 v[44:47], v[172:175], v[180:183], v[44:47]
	v_mfma_f32_16x16x32_bf16 v[32:35], v[164:167], v[188:191], v[32:35]
	v_mfma_f32_16x16x32_bf16 v[28:31], v[172:175], v[188:191], v[28:31]
	v_mfma_f32_16x16x32_bf16 v[16:19], v[164:167], v[196:199], v[16:19]
	v_mfma_f32_16x16x32_bf16 v[12:15], v[172:175], v[196:199], v[12:15]
	v_mfma_f32_16x16x32_bf16 v[8:11], v[164:167], v[204:207], v[8:11]
	v_mfma_f32_16x16x32_bf16 v[4:7], v[172:175], v[204:207], v[4:7]
	v_mfma_f32_16x16x32_bf16 v[48:51], v[168:171], v[184:187], v[48:51]
	v_mfma_f32_16x16x32_bf16 v[44:47], v[176:179], v[184:187], v[44:47]
	v_mfma_f32_16x16x32_bf16 v[32:35], v[168:171], v[192:195], v[32:35]
	v_mfma_f32_16x16x32_bf16 v[28:31], v[176:179], v[192:195], v[28:31]
	v_mfma_f32_16x16x32_bf16 v[16:19], v[168:171], v[200:203], v[16:19]
	v_mfma_f32_16x16x32_bf16 v[12:15], v[176:179], v[200:203], v[12:15]
	v_mfma_f32_16x16x32_bf16 v[8:11], v[168:171], v[218:221], v[8:11]
	v_mfma_f32_16x16x32_bf16 v[4:7], v[176:179], v[218:221], v[4:7]
	s_setprio 0
	s_barrier
	s_add_i32 s91, 0, 0x18000
	s_add_i32 s92, 0, 0x1c000
	v_add_u32_e32 v160, s91, v154
	v_add_u32_e32 v176, s92, v154
	ds_read_b128 v[146:149], v160
	ds_read_b128 v[150:153], v160 offset:1024
	ds_read_b128 v[156:159], v160 offset:2048
	ds_read_b128 v[160:163], v160 offset:3072
	ds_read_b128 v[164:167], v176
	ds_read_b128 v[168:171], v176 offset:1024
	ds_read_b128 v[172:175], v176 offset:2048
	ds_read_b128 v[176:179], v176 offset:3072
	s_add_u32 s44, s44, 0x80000
	s_addc_u32 s45, s45, 0
	s_mov_b32 m0, s80
	ds_read_b128 v[180:183], v155 offset:32768
	ds_read_b128 v[184:187], v155 offset:33792
	ds_read_b128 v[188:191], v155 offset:34816
	ds_read_b128 v[192:195], v155 offset:35840
	ds_read_b128 v[196:199], v155 offset:36864
	ds_read_b128 v[200:203], v155 offset:37888
	ds_read_b128 v[204:207], v155 offset:38912
	ds_read_b128 v[218:221], v155 offset:39936
	global_load_lds_dwordx4 v136, s[44:45]
	s_mov_b32 m0, s81
	s_nop 0
	global_load_lds_dwordx4 v134, s[44:45]
	s_waitcnt vmcnt(8)
	s_waitcnt lgkmcnt(0)
	s_barrier
	s_setprio 1
	s_waitcnt lgkmcnt(0)
	v_mfma_f32_16x16x32_bf16 v[128:131], v[146:149], v[180:183], v[128:131]
	v_mfma_f32_16x16x32_bf16 v[124:127], v[156:159], v[180:183], v[124:127]
	v_mfma_f32_16x16x32_bf16 v[120:123], v[146:149], v[188:191], v[120:123]
	v_mfma_f32_16x16x32_bf16 v[116:119], v[156:159], v[188:191], v[116:119]
	v_mfma_f32_16x16x32_bf16 v[112:115], v[146:149], v[196:199], v[112:115]
	v_mfma_f32_16x16x32_bf16 v[104:107], v[156:159], v[196:199], v[104:107]
	v_mfma_f32_16x16x32_bf16 v[96:99], v[146:149], v[204:207], v[96:99]
	v_mfma_f32_16x16x32_bf16 v[88:91], v[156:159], v[204:207], v[88:91]
	v_mfma_f32_16x16x32_bf16 v[128:131], v[150:153], v[184:187], v[128:131]
	v_mfma_f32_16x16x32_bf16 v[124:127], v[160:163], v[184:187], v[124:127]
	v_mfma_f32_16x16x32_bf16 v[120:123], v[150:153], v[192:195], v[120:123]
	v_mfma_f32_16x16x32_bf16 v[116:119], v[160:163], v[192:195], v[116:119]
	v_mfma_f32_16x16x32_bf16 v[112:115], v[150:153], v[200:203], v[112:115]
	v_mfma_f32_16x16x32_bf16 v[104:107], v[160:163], v[200:203], v[104:107]
	v_mfma_f32_16x16x32_bf16 v[96:99], v[150:153], v[218:221], v[96:99]
	v_mfma_f32_16x16x32_bf16 v[88:91], v[160:163], v[218:221], v[88:91]
	s_setprio 0
	s_setprio 1
	v_mfma_f32_16x16x32_bf16 v[108:111], v[164:167], v[180:183], v[108:111]
	v_mfma_f32_16x16x32_bf16 v[100:103], v[172:175], v[180:183], v[100:103]
	v_mfma_f32_16x16x32_bf16 v[92:95], v[164:167], v[188:191], v[92:95]
	v_mfma_f32_16x16x32_bf16 v[84:87], v[172:175], v[188:191], v[84:87]
	v_mfma_f32_16x16x32_bf16 v[80:83], v[164:167], v[196:199], v[80:83]
	v_mfma_f32_16x16x32_bf16 v[76:79], v[172:175], v[196:199], v[76:79]
	v_mfma_f32_16x16x32_bf16 v[72:75], v[164:167], v[204:207], v[72:75]
	v_mfma_f32_16x16x32_bf16 v[68:71], v[172:175], v[204:207], v[68:71]
	v_mfma_f32_16x16x32_bf16 v[108:111], v[168:171], v[184:187], v[108:111]
	v_mfma_f32_16x16x32_bf16 v[100:103], v[176:179], v[184:187], v[100:103]
	v_mfma_f32_16x16x32_bf16 v[92:95], v[168:171], v[192:195], v[92:95]
	v_mfma_f32_16x16x32_bf16 v[84:87], v[176:179], v[192:195], v[84:87]
	v_mfma_f32_16x16x32_bf16 v[80:83], v[168:171], v[200:203], v[80:83]
	v_mfma_f32_16x16x32_bf16 v[76:79], v[176:179], v[200:203], v[76:79]
	v_mfma_f32_16x16x32_bf16 v[72:75], v[168:171], v[218:221], v[72:75]
	v_mfma_f32_16x16x32_bf16 v[68:71], v[176:179], v[218:221], v[68:71]
	s_setprio 0
	s_barrier
	s_add_i32 s44, s91, s51
	s_mov_b32 m0, s44
	ds_read_b128 v[180:183], v155 offset:49152
	ds_read_b128 v[184:187], v155 offset:50176
	ds_read_b128 v[188:191], v155 offset:51200
	ds_read_b128 v[192:195], v155 offset:52224
	ds_read_b128 v[196:199], v155 offset:53248
	ds_read_b128 v[200:203], v155 offset:54272
	ds_read_b128 v[204:207], v155 offset:55296
	ds_read_b128 v[218:221], v155 offset:56320
	global_load_lds_dwordx4 v2, s[98:99]
	s_add_i32 m0, s44, 0x2000
	s_add_u32 s42, s42, 0x80080
	s_addc_u32 s43, s43, 0
	s_add_i32 s44, s92, s51
	global_load_lds_dwordx4 v132, s[98:99]
	s_mov_b32 m0, s44
	s_nop 0
	global_load_lds_dwordx4 v2, s[42:43]
	s_add_i32 m0, s44, 0x2000
	s_nop 0
	global_load_lds_dwordx4 v132, s[42:43]
	s_mov_b32 m0, s82
	s_nop 0
	global_load_lds_dwordx4 v136, vcc
	s_mov_b32 m0, s83
	s_nop 0
	global_load_lds_dwordx4 v134, vcc
	s_waitcnt vmcnt(8)
	s_waitcnt lgkmcnt(0)
	s_barrier
	s_setprio 1
	s_waitcnt lgkmcnt(0)
	v_mfma_f32_16x16x32_bf16 v[64:67], v[146:149], v[180:183], v[64:67]
	v_mfma_f32_16x16x32_bf16 v[60:63], v[156:159], v[180:183], v[60:63]
	v_mfma_f32_16x16x32_bf16 v[56:59], v[146:149], v[188:191], v[56:59]
	v_mfma_f32_16x16x32_bf16 v[52:55], v[156:159], v[188:191], v[52:55]
	v_mfma_f32_16x16x32_bf16 v[40:43], v[146:149], v[196:199], v[40:43]
	v_mfma_f32_16x16x32_bf16 v[36:39], v[156:159], v[196:199], v[36:39]
	v_mfma_f32_16x16x32_bf16 v[24:27], v[146:149], v[204:207], v[24:27]
	v_mfma_f32_16x16x32_bf16 v[20:23], v[156:159], v[204:207], v[20:23]
	v_mfma_f32_16x16x32_bf16 v[64:67], v[150:153], v[184:187], v[64:67]
	v_mfma_f32_16x16x32_bf16 v[60:63], v[160:163], v[184:187], v[60:63]
	v_mfma_f32_16x16x32_bf16 v[56:59], v[150:153], v[192:195], v[56:59]
	v_mfma_f32_16x16x32_bf16 v[52:55], v[160:163], v[192:195], v[52:55]
	v_mfma_f32_16x16x32_bf16 v[40:43], v[150:153], v[200:203], v[40:43]
	v_mfma_f32_16x16x32_bf16 v[36:39], v[160:163], v[200:203], v[36:39]
	v_mfma_f32_16x16x32_bf16 v[24:27], v[150:153], v[218:221], v[24:27]
	v_mfma_f32_16x16x32_bf16 v[20:23], v[160:163], v[218:221], v[20:23]
	s_setprio 0
	s_setprio 1
	v_mfma_f32_16x16x32_bf16 v[48:51], v[164:167], v[180:183], v[48:51]
	v_mfma_f32_16x16x32_bf16 v[44:47], v[172:175], v[180:183], v[44:47]
	v_mfma_f32_16x16x32_bf16 v[32:35], v[164:167], v[188:191], v[32:35]
	v_mfma_f32_16x16x32_bf16 v[28:31], v[172:175], v[188:191], v[28:31]
	v_mfma_f32_16x16x32_bf16 v[16:19], v[164:167], v[196:199], v[16:19]
	v_mfma_f32_16x16x32_bf16 v[12:15], v[172:175], v[196:199], v[12:15]
	v_mfma_f32_16x16x32_bf16 v[8:11], v[164:167], v[204:207], v[8:11]
	v_mfma_f32_16x16x32_bf16 v[4:7], v[172:175], v[204:207], v[4:7]
	v_mfma_f32_16x16x32_bf16 v[48:51], v[168:171], v[184:187], v[48:51]
	v_mfma_f32_16x16x32_bf16 v[44:47], v[176:179], v[184:187], v[44:47]
	v_mfma_f32_16x16x32_bf16 v[32:35], v[168:171], v[192:195], v[32:35]
	v_mfma_f32_16x16x32_bf16 v[28:31], v[176:179], v[192:195], v[28:31]
	v_mfma_f32_16x16x32_bf16 v[16:19], v[168:171], v[200:203], v[16:19]
	v_mfma_f32_16x16x32_bf16 v[12:15], v[176:179], v[200:203], v[12:15]
	v_mfma_f32_16x16x32_bf16 v[8:11], v[168:171], v[218:221], v[8:11]
	v_mfma_f32_16x16x32_bf16 v[4:7], v[176:179], v[218:221], v[4:7]
	s_setprio 0
	s_barrier
	s_add_i32 s90, s90, 2
	s_add_u32 s40, s40, 0x100
	s_addc_u32 s41, s41, 0
	s_add_u32 s88, s88, 0x100
	s_addc_u32 s89, s89, 0
	s_cmp_gt_u32 s90, 29
	s_cbranch_scc0 .LBB0_191
	s_and_b64 vcc, exec, s[6:7]
	s_cbranch_vccz .LBB0_194
	s_barrier

.LBB0_661:
	s_add_u32 s42, s40, 0xfffc0080
	s_addc_u32 s43, s41, -1
	s_add_i32 s89, 0, 0x10000
	s_cmp_eq_u32 s88, 12
	s_cselect_b32 s45, s37, s43
	s_cselect_b32 s44, s36, s42
	s_cselect_b32 s43, s11, s87
	s_cselect_b32 s42, s13, s86
	s_add_i32 s92, 0, 0x14000
	v_add_u32_e32 v158, s89, v144
	v_add_u32_e32 v174, s92, v144
	ds_read_b128 v[146:149], v158
	ds_read_b128 v[150:153], v158 offset:1024
	ds_read_b128 v[154:157], v158 offset:2048
	ds_read_b128 v[158:161], v158 offset:3072
	ds_read_b128 v[162:165], v174
	ds_read_b128 v[166:169], v174 offset:1024
	ds_read_b128 v[170:173], v174 offset:2048
	ds_read_b128 v[174:177], v174 offset:3072
	s_add_i32 m0, s51, 0xc000
	ds_read_b128 v[178:181], v145
	ds_read_b128 v[182:185], v145 offset:1024
	ds_read_b128 v[186:189], v145 offset:2048
	ds_read_b128 v[190:193], v145 offset:3072
	ds_read_b128 v[194:197], v145 offset:4096
	ds_read_b128 v[198:201], v145 offset:5120
	ds_read_b128 v[202:205], v145 offset:6144
	ds_read_b128 v[218:221], v145 offset:7168
	global_load_lds_dwordx4 v140, s[40:41]
	s_add_i32 m0, s51, 0xe000
	s_nop 0
	global_load_lds_dwordx4 v142, s[40:41]
	s_waitcnt vmcnt(8)
	s_waitcnt lgkmcnt(0)
	s_barrier
	s_setprio 1
	s_waitcnt lgkmcnt(0)
	v_mfma_f32_16x16x32_bf16 v[128:131], v[146:149], v[178:181], v[128:131]
	v_mfma_f32_16x16x32_bf16 v[124:127], v[154:157], v[178:181], v[124:127]
	v_mfma_f32_16x16x32_bf16 v[120:123], v[146:149], v[186:189], v[120:123]
	v_mfma_f32_16x16x32_bf16 v[116:119], v[154:157], v[186:189], v[116:119]
	v_mfma_f32_16x16x32_bf16 v[104:107], v[146:149], v[194:197], v[104:107]
	v_mfma_f32_16x16x32_bf16 v[100:103], v[154:157], v[194:197], v[100:103]
	v_mfma_f32_16x16x32_bf16 v[88:91], v[146:149], v[202:205], v[88:91]
	v_mfma_f32_16x16x32_bf16 v[84:87], v[154:157], v[202:205], v[84:87]
	v_mfma_f32_16x16x32_bf16 v[128:131], v[150:153], v[182:185], v[128:131]
	v_mfma_f32_16x16x32_bf16 v[124:127], v[158:161], v[182:185], v[124:127]
	v_mfma_f32_16x16x32_bf16 v[120:123], v[150:153], v[190:193], v[120:123]
	v_mfma_f32_16x16x32_bf16 v[116:119], v[158:161], v[190:193], v[116:119]
	v_mfma_f32_16x16x32_bf16 v[104:107], v[150:153], v[198:201], v[104:107]
	v_mfma_f32_16x16x32_bf16 v[100:103], v[158:161], v[198:201], v[100:103]
	v_mfma_f32_16x16x32_bf16 v[88:91], v[150:153], v[218:221], v[88:91]
	v_mfma_f32_16x16x32_bf16 v[84:87], v[158:161], v[218:221], v[84:87]
	s_setprio 0
	s_setprio 1
	v_mfma_f32_16x16x32_bf16 v[112:115], v[162:165], v[178:181], v[112:115]
	v_mfma_f32_16x16x32_bf16 v[108:111], v[170:173], v[178:181], v[108:111]
	v_mfma_f32_16x16x32_bf16 v[96:99], v[162:165], v[186:189], v[96:99]
	v_mfma_f32_16x16x32_bf16 v[92:95], v[170:173], v[186:189], v[92:95]
	v_mfma_f32_16x16x32_bf16 v[80:83], v[162:165], v[194:197], v[80:83]
	v_mfma_f32_16x16x32_bf16 v[76:79], v[170:173], v[194:197], v[76:79]
	v_mfma_f32_16x16x32_bf16 v[72:75], v[162:165], v[202:205], v[72:75]
	v_mfma_f32_16x16x32_bf16 v[68:71], v[170:173], v[202:205], v[68:71]
	v_mfma_f32_16x16x32_bf16 v[112:115], v[166:169], v[182:185], v[112:115]
	v_mfma_f32_16x16x32_bf16 v[108:111], v[174:177], v[182:185], v[108:111]
	v_mfma_f32_16x16x32_bf16 v[96:99], v[166:169], v[190:193], v[96:99]
	v_mfma_f32_16x16x32_bf16 v[92:95], v[174:177], v[190:193], v[92:95]
	v_mfma_f32_16x16x32_bf16 v[80:83], v[166:169], v[198:201], v[80:83]
	v_mfma_f32_16x16x32_bf16 v[76:79], v[174:177], v[198:201], v[76:79]
	v_mfma_f32_16x16x32_bf16 v[72:75], v[166:169], v[218:221], v[72:75]
	v_mfma_f32_16x16x32_bf16 v[68:71], v[174:177], v[218:221], v[68:71]
	s_setprio 0
	s_barrier
	s_add_i32 s89, s89, s49
	s_mov_b32 m0, s89
	ds_read_b128 v[178:181], v145 offset:16384
	ds_read_b128 v[182:185], v145 offset:17408
	ds_read_b128 v[186:189], v145 offset:18432
	ds_read_b128 v[190:193], v145 offset:19456
	ds_read_b128 v[194:197], v145 offset:20480
	ds_read_b128 v[198:201], v145 offset:21504
	ds_read_b128 v[202:205], v145 offset:22528
	ds_read_b128 v[218:221], v145 offset:23552
	global_load_lds_dwordx4 v136, s[42:43]
	s_add_i32 m0, s89, 0x2000
	s_add_u32 s90, s42, 0x40000
	s_addc_u32 s91, s43, 0
	s_add_i32 s89, s92, s49
	global_load_lds_dwordx4 v132, s[42:43]
	s_mov_b32 m0, s89
	s_nop 0
	global_load_lds_dwordx4 v136, s[90:91]
	s_add_i32 m0, s89, 0x2000
	s_nop 0
	global_load_lds_dwordx4 v132, s[90:91]
	s_mov_b32 m0, s51
	s_nop 0
	global_load_lds_dwordx4 v138, s[44:45]
	s_mov_b32 m0, s60
	s_nop 0
	global_load_lds_dwordx4 v134, s[44:45]
	s_add_u32 s98, s42, s16
	s_addc_u32 s99, s43, s17
	s_add_u32 vcc_lo, s44, s16
	s_addc_u32 vcc_hi, s45, s17
	s_waitcnt vmcnt(8)
	s_waitcnt lgkmcnt(0)
	s_barrier
	s_setprio 1
	s_waitcnt lgkmcnt(0)
	v_mfma_f32_16x16x32_bf16 v[64:67], v[146:149], v[178:181], v[64:67]
	v_mfma_f32_16x16x32_bf16 v[60:63], v[154:157], v[178:181], v[60:63]
	v_mfma_f32_16x16x32_bf16 v[56:59], v[146:149], v[186:189], v[56:59]
	v_mfma_f32_16x16x32_bf16 v[52:55], v[154:157], v[186:189], v[52:55]
	v_mfma_f32_16x16x32_bf16 v[40:43], v[146:149], v[194:197], v[40:43]
	v_mfma_f32_16x16x32_bf16 v[36:39], v[154:157], v[194:197], v[36:39]
	v_mfma_f32_16x16x32_bf16 v[24:27], v[146:149], v[202:205], v[24:27]
	v_mfma_f32_16x16x32_bf16 v[20:23], v[154:157], v[202:205], v[20:23]
	v_mfma_f32_16x16x32_bf16 v[64:67], v[150:153], v[182:185], v[64:67]
	v_mfma_f32_16x16x32_bf16 v[60:63], v[158:161], v[182:185], v[60:63]
	v_mfma_f32_16x16x32_bf16 v[56:59], v[150:153], v[190:193], v[56:59]
	v_mfma_f32_16x16x32_bf16 v[52:55], v[158:161], v[190:193], v[52:55]
	v_mfma_f32_16x16x32_bf16 v[40:43], v[150:153], v[198:201], v[40:43]
	v_mfma_f32_16x16x32_bf16 v[36:39], v[158:161], v[198:201], v[36:39]
	v_mfma_f32_16x16x32_bf16 v[24:27], v[150:153], v[218:221], v[24:27]
	v_mfma_f32_16x16x32_bf16 v[20:23], v[158:161], v[218:221], v[20:23]
	s_setprio 0
	s_setprio 1
	v_mfma_f32_16x16x32_bf16 v[48:51], v[162:165], v[178:181], v[48:51]
	v_mfma_f32_16x16x32_bf16 v[44:47], v[170:173], v[178:181], v[44:47]
	v_mfma_f32_16x16x32_bf16 v[32:35], v[162:165], v[186:189], v[32:35]
	v_mfma_f32_16x16x32_bf16 v[28:31], v[170:173], v[186:189], v[28:31]
	v_mfma_f32_16x16x32_bf16 v[16:19], v[162:165], v[194:197], v[16:19]
	v_mfma_f32_16x16x32_bf16 v[12:15], v[170:173], v[194:197], v[12:15]
	v_mfma_f32_16x16x32_bf16 v[8:11], v[162:165], v[202:205], v[8:11]
	v_mfma_f32_16x16x32_bf16 v[4:7], v[170:173], v[202:205], v[4:7]
	v_mfma_f32_16x16x32_bf16 v[48:51], v[166:169], v[182:185], v[48:51]
	v_mfma_f32_16x16x32_bf16 v[44:47], v[174:177], v[182:185], v[44:47]
	v_mfma_f32_16x16x32_bf16 v[32:35], v[166:169], v[190:193], v[32:35]
	v_mfma_f32_16x16x32_bf16 v[28:31], v[174:177], v[190:193], v[28:31]
	v_mfma_f32_16x16x32_bf16 v[16:19], v[166:169], v[198:201], v[16:19]
	v_mfma_f32_16x16x32_bf16 v[12:15], v[174:177], v[198:201], v[12:15]
	v_mfma_f32_16x16x32_bf16 v[8:11], v[166:169], v[218:221], v[8:11]
	v_mfma_f32_16x16x32_bf16 v[4:7], v[174:177], v[218:221], v[4:7]
	s_setprio 0
	s_barrier
	s_add_i32 s89, 0, 0x18000
	s_add_i32 s90, 0, 0x1c000
	v_add_u32_e32 v158, s89, v144
	v_add_u32_e32 v174, s90, v144
	ds_read_b128 v[146:149], v158
	ds_read_b128 v[150:153], v158 offset:1024
	ds_read_b128 v[154:157], v158 offset:2048
	ds_read_b128 v[158:161], v158 offset:3072
	ds_read_b128 v[162:165], v174
	ds_read_b128 v[166:169], v174 offset:1024
	ds_read_b128 v[170:173], v174 offset:2048
	ds_read_b128 v[174:177], v174 offset:3072
	s_add_u32 s44, s44, 0x40000
	s_addc_u32 s45, s45, 0
	s_mov_b32 m0, s61
	ds_read_b128 v[178:181], v145 offset:32768
	ds_read_b128 v[182:185], v145 offset:33792
	ds_read_b128 v[186:189], v145 offset:34816
	ds_read_b128 v[190:193], v145 offset:35840
	ds_read_b128 v[194:197], v145 offset:36864
	ds_read_b128 v[198:201], v145 offset:37888
	ds_read_b128 v[202:205], v145 offset:38912
	ds_read_b128 v[218:221], v145 offset:39936
	global_load_lds_dwordx4 v138, s[44:45]
	s_mov_b32 m0, s80
	s_nop 0
	global_load_lds_dwordx4 v134, s[44:45]
	s_waitcnt vmcnt(8)
	s_waitcnt lgkmcnt(0)
	s_barrier
	s_setprio 1
	s_waitcnt lgkmcnt(0)
	v_mfma_f32_16x16x32_bf16 v[128:131], v[146:149], v[178:181], v[128:131]
	v_mfma_f32_16x16x32_bf16 v[124:127], v[154:157], v[178:181], v[124:127]
	v_mfma_f32_16x16x32_bf16 v[120:123], v[146:149], v[186:189], v[120:123]
	v_mfma_f32_16x16x32_bf16 v[116:119], v[154:157], v[186:189], v[116:119]
	v_mfma_f32_16x16x32_bf16 v[104:107], v[146:149], v[194:197], v[104:107]
	v_mfma_f32_16x16x32_bf16 v[100:103], v[154:157], v[194:197], v[100:103]
	v_mfma_f32_16x16x32_bf16 v[88:91], v[146:149], v[202:205], v[88:91]
	v_mfma_f32_16x16x32_bf16 v[84:87], v[154:157], v[202:205], v[84:87]
	v_mfma_f32_16x16x32_bf16 v[128:131], v[150:153], v[182:185], v[128:131]
	v_mfma_f32_16x16x32_bf16 v[124:127], v[158:161], v[182:185], v[124:127]
	v_mfma_f32_16x16x32_bf16 v[120:123], v[150:153], v[190:193], v[120:123]
	v_mfma_f32_16x16x32_bf16 v[116:119], v[158:161], v[190:193], v[116:119]
	v_mfma_f32_16x16x32_bf16 v[104:107], v[150:153], v[198:201], v[104:107]
	v_mfma_f32_16x16x32_bf16 v[100:103], v[158:161], v[198:201], v[100:103]
	v_mfma_f32_16x16x32_bf16 v[88:91], v[150:153], v[218:221], v[88:91]
	v_mfma_f32_16x16x32_bf16 v[84:87], v[158:161], v[218:221], v[84:87]
	s_setprio 0
	s_setprio 1
	v_mfma_f32_16x16x32_bf16 v[112:115], v[162:165], v[178:181], v[112:115]
	v_mfma_f32_16x16x32_bf16 v[108:111], v[170:173], v[178:181], v[108:111]
	v_mfma_f32_16x16x32_bf16 v[96:99], v[162:165], v[186:189], v[96:99]
	v_mfma_f32_16x16x32_bf16 v[92:95], v[170:173], v[186:189], v[92:95]
	v_mfma_f32_16x16x32_bf16 v[80:83], v[162:165], v[194:197], v[80:83]
	v_mfma_f32_16x16x32_bf16 v[76:79], v[170:173], v[194:197], v[76:79]
	v_mfma_f32_16x16x32_bf16 v[72:75], v[162:165], v[202:205], v[72:75]
	v_mfma_f32_16x16x32_bf16 v[68:71], v[170:173], v[202:205], v[68:71]
	v_mfma_f32_16x16x32_bf16 v[112:115], v[166:169], v[182:185], v[112:115]
	v_mfma_f32_16x16x32_bf16 v[108:111], v[174:177], v[182:185], v[108:111]
	v_mfma_f32_16x16x32_bf16 v[96:99], v[166:169], v[190:193], v[96:99]
	v_mfma_f32_16x16x32_bf16 v[92:95], v[174:177], v[190:193], v[92:95]
	v_mfma_f32_16x16x32_bf16 v[80:83], v[166:169], v[198:201], v[80:83]
	v_mfma_f32_16x16x32_bf16 v[76:79], v[174:177], v[198:201], v[76:79]
	v_mfma_f32_16x16x32_bf16 v[72:75], v[166:169], v[218:221], v[72:75]
	v_mfma_f32_16x16x32_bf16 v[68:71], v[174:177], v[218:221], v[68:71]
	s_setprio 0
	s_barrier
	s_add_i32 s44, s89, s49
	s_mov_b32 m0, s44
	ds_read_b128 v[178:181], v145 offset:49152
	ds_read_b128 v[182:185], v145 offset:50176
	ds_read_b128 v[186:189], v145 offset:51200
	ds_read_b128 v[190:193], v145 offset:52224
	ds_read_b128 v[194:197], v145 offset:53248
	ds_read_b128 v[198:201], v145 offset:54272
	ds_read_b128 v[202:205], v145 offset:55296
	ds_read_b128 v[218:221], v145 offset:56320
	global_load_lds_dwordx4 v136, s[98:99]
	s_add_i32 m0, s44, 0x2000
	s_add_u32 s42, s42, 0x40080
	s_addc_u32 s43, s43, 0
	s_add_i32 s44, s90, s49
	global_load_lds_dwordx4 v132, s[98:99]
	s_mov_b32 m0, s44
	s_nop 0
	global_load_lds_dwordx4 v136, s[42:43]
	s_add_i32 m0, s44, 0x2000
	s_nop 0
	global_load_lds_dwordx4 v132, s[42:43]
	s_mov_b32 m0, s81
	s_nop 0
	global_load_lds_dwordx4 v138, vcc
	s_mov_b32 m0, s82
	s_nop 0
	global_load_lds_dwordx4 v134, vcc
	s_waitcnt vmcnt(8)
	s_waitcnt lgkmcnt(0)
	s_barrier
	s_setprio 1
	s_waitcnt lgkmcnt(0)
	v_mfma_f32_16x16x32_bf16 v[64:67], v[146:149], v[178:181], v[64:67]
	v_mfma_f32_16x16x32_bf16 v[60:63], v[154:157], v[178:181], v[60:63]
	v_mfma_f32_16x16x32_bf16 v[56:59], v[146:149], v[186:189], v[56:59]
	v_mfma_f32_16x16x32_bf16 v[52:55], v[154:157], v[186:189], v[52:55]
	v_mfma_f32_16x16x32_bf16 v[40:43], v[146:149], v[194:197], v[40:43]
	v_mfma_f32_16x16x32_bf16 v[36:39], v[154:157], v[194:197], v[36:39]
	v_mfma_f32_16x16x32_bf16 v[24:27], v[146:149], v[202:205], v[24:27]
	v_mfma_f32_16x16x32_bf16 v[20:23], v[154:157], v[202:205], v[20:23]
	v_mfma_f32_16x16x32_bf16 v[64:67], v[150:153], v[182:185], v[64:67]
	v_mfma_f32_16x16x32_bf16 v[60:63], v[158:161], v[182:185], v[60:63]
	v_mfma_f32_16x16x32_bf16 v[56:59], v[150:153], v[190:193], v[56:59]
	v_mfma_f32_16x16x32_bf16 v[52:55], v[158:161], v[190:193], v[52:55]
	v_mfma_f32_16x16x32_bf16 v[40:43], v[150:153], v[198:201], v[40:43]
	v_mfma_f32_16x16x32_bf16 v[36:39], v[158:161], v[198:201], v[36:39]
	v_mfma_f32_16x16x32_bf16 v[24:27], v[150:153], v[218:221], v[24:27]
	v_mfma_f32_16x16x32_bf16 v[20:23], v[158:161], v[218:221], v[20:23]
	s_setprio 0
	s_setprio 1
	v_mfma_f32_16x16x32_bf16 v[48:51], v[162:165], v[178:181], v[48:51]
	v_mfma_f32_16x16x32_bf16 v[44:47], v[170:173], v[178:181], v[44:47]
	v_mfma_f32_16x16x32_bf16 v[32:35], v[162:165], v[186:189], v[32:35]
	v_mfma_f32_16x16x32_bf16 v[28:31], v[170:173], v[186:189], v[28:31]
	v_mfma_f32_16x16x32_bf16 v[16:19], v[162:165], v[194:197], v[16:19]
	v_mfma_f32_16x16x32_bf16 v[12:15], v[170:173], v[194:197], v[12:15]
	v_mfma_f32_16x16x32_bf16 v[8:11], v[162:165], v[202:205], v[8:11]
	v_mfma_f32_16x16x32_bf16 v[4:7], v[170:173], v[202:205], v[4:7]
	v_mfma_f32_16x16x32_bf16 v[48:51], v[166:169], v[182:185], v[48:51]
	v_mfma_f32_16x16x32_bf16 v[44:47], v[174:177], v[182:185], v[44:47]
	v_mfma_f32_16x16x32_bf16 v[32:35], v[166:169], v[190:193], v[32:35]
	v_mfma_f32_16x16x32_bf16 v[28:31], v[174:177], v[190:193], v[28:31]
	v_mfma_f32_16x16x32_bf16 v[16:19], v[166:169], v[198:201], v[16:19]
	v_mfma_f32_16x16x32_bf16 v[12:15], v[174:177], v[198:201], v[12:15]
	v_mfma_f32_16x16x32_bf16 v[8:11], v[166:169], v[218:221], v[8:11]
	v_mfma_f32_16x16x32_bf16 v[4:7], v[174:177], v[218:221], v[4:7]
	s_setprio 0
	s_barrier
	s_add_i32 s88, s88, 2
	s_add_u32 s40, s40, 0x100
	s_addc_u32 s41, s41, 0
	s_add_u32 s86, s86, 0x100
	s_addc_u32 s87, s87, 0
	s_cmp_gt_u32 s88, 13
	s_cbranch_scc0 .LBB0_661
	s_and_b64 vcc, exec, s[8:9]
	s_cbranch_vccz .LBB0_664
	s_barrier

.LBB0_732:
	s_add_u32 s40, s38, 0xfff80080
	s_addc_u32 s41, s39, -1
	s_add_i32 s89, 0, 0x10000
	s_cmp_eq_u32 s88, 28
	s_cselect_b32 s43, s9, s41
	s_cselect_b32 s42, s84, s40
	v_add_u32_e32 v2, s89, v1
	s_cselect_b32 s41, s11, s87
	s_cselect_b32 s40, s85, s86
	s_add_i32 s92, 0, 0x14000
	ds_read_b128 v[144:147], v2
	ds_read_b128 v[148:151], v2 offset:1024
	ds_read_b128 v[152:155], v2 offset:2048
	ds_read_b128 v[156:159], v2 offset:3072
	v_add_u32_e32 v2, s92, v1
	ds_read_b128 v[160:163], v2
	ds_read_b128 v[164:167], v2 offset:1024
	ds_read_b128 v[168:171], v2 offset:2048
	ds_read_b128 v[172:175], v2 offset:3072
	s_add_i32 m0, s48, 0xc000
	ds_read_b128 v[176:179], v219
	ds_read_b128 v[180:183], v219 offset:1024
	ds_read_b128 v[184:187], v219 offset:2048
	ds_read_b128 v[188:191], v219 offset:3072
	ds_read_b128 v[192:195], v219 offset:4096
	ds_read_b128 v[196:199], v219 offset:5120
	ds_read_b128 v[200:203], v219 offset:6144
	ds_read_b128 v[204:207], v219 offset:7168
	global_load_lds_dwordx4 v140, s[38:39]
	s_add_i32 m0, s48, 0xe000
	s_nop 0
	global_load_lds_dwordx4 v142, s[38:39]
	s_waitcnt vmcnt(8)
	s_waitcnt lgkmcnt(0)
	s_barrier
	s_setprio 1
	s_waitcnt lgkmcnt(0)
	v_mfma_f32_16x16x32_bf16 v[128:131], v[144:147], v[176:179], v[128:131]
	v_mfma_f32_16x16x32_bf16 v[124:127], v[152:155], v[176:179], v[124:127]
	v_mfma_f32_16x16x32_bf16 v[112:115], v[144:147], v[184:187], v[112:115]
	v_mfma_f32_16x16x32_bf16 v[108:111], v[152:155], v[184:187], v[108:111]
	v_mfma_f32_16x16x32_bf16 v[96:99], v[144:147], v[192:195], v[96:99]
	v_mfma_f32_16x16x32_bf16 v[92:95], v[152:155], v[192:195], v[92:95]
	v_mfma_f32_16x16x32_bf16 v[80:83], v[144:147], v[200:203], v[80:83]
	v_mfma_f32_16x16x32_bf16 v[76:79], v[152:155], v[200:203], v[76:79]
	v_mfma_f32_16x16x32_bf16 v[128:131], v[148:151], v[180:183], v[128:131]
	v_mfma_f32_16x16x32_bf16 v[124:127], v[156:159], v[180:183], v[124:127]
	v_mfma_f32_16x16x32_bf16 v[112:115], v[148:151], v[188:191], v[112:115]
	v_mfma_f32_16x16x32_bf16 v[108:111], v[156:159], v[188:191], v[108:111]
	v_mfma_f32_16x16x32_bf16 v[96:99], v[148:151], v[196:199], v[96:99]
	v_mfma_f32_16x16x32_bf16 v[92:95], v[156:159], v[196:199], v[92:95]
	v_mfma_f32_16x16x32_bf16 v[80:83], v[148:151], v[204:207], v[80:83]
	v_mfma_f32_16x16x32_bf16 v[76:79], v[156:159], v[204:207], v[76:79]
	s_setprio 0
	s_setprio 1
	v_mfma_f32_16x16x32_bf16 v[120:123], v[160:163], v[176:179], v[120:123]
	v_mfma_f32_16x16x32_bf16 v[116:119], v[168:171], v[176:179], v[116:119]
	v_mfma_f32_16x16x32_bf16 v[104:107], v[160:163], v[184:187], v[104:107]
	v_mfma_f32_16x16x32_bf16 v[100:103], v[168:171], v[184:187], v[100:103]
	v_mfma_f32_16x16x32_bf16 v[88:91], v[160:163], v[192:195], v[88:91]
	v_mfma_f32_16x16x32_bf16 v[84:87], v[168:171], v[192:195], v[84:87]
	v_mfma_f32_16x16x32_bf16 v[72:75], v[160:163], v[200:203], v[72:75]
	v_mfma_f32_16x16x32_bf16 v[68:71], v[168:171], v[200:203], v[68:71]
	v_mfma_f32_16x16x32_bf16 v[120:123], v[164:167], v[180:183], v[120:123]
	v_mfma_f32_16x16x32_bf16 v[116:119], v[172:175], v[180:183], v[116:119]
	v_mfma_f32_16x16x32_bf16 v[104:107], v[164:167], v[188:191], v[104:107]
	v_mfma_f32_16x16x32_bf16 v[100:103], v[172:175], v[188:191], v[100:103]
	v_mfma_f32_16x16x32_bf16 v[88:91], v[164:167], v[196:199], v[88:91]
	v_mfma_f32_16x16x32_bf16 v[84:87], v[172:175], v[196:199], v[84:87]
	v_mfma_f32_16x16x32_bf16 v[72:75], v[164:167], v[204:207], v[72:75]
	v_mfma_f32_16x16x32_bf16 v[68:71], v[172:175], v[204:207], v[68:71]
	s_setprio 0
	s_barrier
	s_add_i32 s89, s89, s45
	s_mov_b32 m0, s89
	ds_read_b128 v[176:179], v219 offset:16384
	ds_read_b128 v[180:183], v219 offset:17408
	ds_read_b128 v[184:187], v219 offset:18432
	ds_read_b128 v[188:191], v219 offset:19456
	ds_read_b128 v[192:195], v219 offset:20480
	ds_read_b128 v[196:199], v219 offset:21504
	ds_read_b128 v[200:203], v219 offset:22528
	ds_read_b128 v[204:207], v219 offset:23552
	global_load_lds_dwordx4 v136, s[40:41]
	s_add_i32 m0, s89, 0x2000
	s_add_u32 s90, s40, 0x80000
	s_addc_u32 s91, s41, 0
	s_add_i32 s89, s92, s45
	global_load_lds_dwordx4 v132, s[40:41]
	s_mov_b32 m0, s89
	s_nop 0
	global_load_lds_dwordx4 v136, s[90:91]
	s_add_i32 m0, s89, 0x2000
	s_nop 0
	global_load_lds_dwordx4 v132, s[90:91]
	s_mov_b32 m0, s48
	s_nop 0
	global_load_lds_dwordx4 v138, s[42:43]
	s_mov_b32 m0, s49
	s_nop 0
	global_load_lds_dwordx4 v134, s[42:43]
	s_add_u32 s98, s40, s16
	s_addc_u32 s99, s41, s17
	s_add_u32 vcc_lo, s42, s16
	s_addc_u32 vcc_hi, s43, s17
	s_waitcnt vmcnt(8)
	s_waitcnt lgkmcnt(0)
	s_barrier
	s_setprio 1
	s_waitcnt lgkmcnt(0)
	v_mfma_f32_16x16x32_bf16 v[64:67], v[144:147], v[176:179], v[64:67]
	v_mfma_f32_16x16x32_bf16 v[60:63], v[152:155], v[176:179], v[60:63]
	v_mfma_f32_16x16x32_bf16 v[48:51], v[144:147], v[184:187], v[48:51]
	v_mfma_f32_16x16x32_bf16 v[44:47], v[152:155], v[184:187], v[44:47]
	v_mfma_f32_16x16x32_bf16 v[32:35], v[144:147], v[192:195], v[32:35]
	v_mfma_f32_16x16x32_bf16 v[28:31], v[152:155], v[192:195], v[28:31]
	v_mfma_f32_16x16x32_bf16 v[16:19], v[144:147], v[200:203], v[16:19]
	v_mfma_f32_16x16x32_bf16 v[12:15], v[152:155], v[200:203], v[12:15]
	v_mfma_f32_16x16x32_bf16 v[64:67], v[148:151], v[180:183], v[64:67]
	v_mfma_f32_16x16x32_bf16 v[60:63], v[156:159], v[180:183], v[60:63]
	v_mfma_f32_16x16x32_bf16 v[48:51], v[148:151], v[188:191], v[48:51]
	v_mfma_f32_16x16x32_bf16 v[44:47], v[156:159], v[188:191], v[44:47]
	v_mfma_f32_16x16x32_bf16 v[32:35], v[148:151], v[196:199], v[32:35]
	v_mfma_f32_16x16x32_bf16 v[28:31], v[156:159], v[196:199], v[28:31]
	v_mfma_f32_16x16x32_bf16 v[16:19], v[148:151], v[204:207], v[16:19]
	v_mfma_f32_16x16x32_bf16 v[12:15], v[156:159], v[204:207], v[12:15]
	s_setprio 0
	s_setprio 1
	v_mfma_f32_16x16x32_bf16 v[56:59], v[160:163], v[176:179], v[56:59]
	v_mfma_f32_16x16x32_bf16 v[52:55], v[168:171], v[176:179], v[52:55]
	v_mfma_f32_16x16x32_bf16 v[40:43], v[160:163], v[184:187], v[40:43]
	v_mfma_f32_16x16x32_bf16 v[36:39], v[168:171], v[184:187], v[36:39]
	v_mfma_f32_16x16x32_bf16 v[24:27], v[160:163], v[192:195], v[24:27]
	v_mfma_f32_16x16x32_bf16 v[20:23], v[168:171], v[192:195], v[20:23]
	v_mfma_f32_16x16x32_bf16 v[8:11], v[160:163], v[200:203], v[8:11]
	v_mfma_f32_16x16x32_bf16 v[4:7], v[168:171], v[200:203], v[4:7]
	v_mfma_f32_16x16x32_bf16 v[56:59], v[164:167], v[180:183], v[56:59]
	v_mfma_f32_16x16x32_bf16 v[52:55], v[172:175], v[180:183], v[52:55]
	v_mfma_f32_16x16x32_bf16 v[40:43], v[164:167], v[188:191], v[40:43]
	v_mfma_f32_16x16x32_bf16 v[36:39], v[172:175], v[188:191], v[36:39]
	v_mfma_f32_16x16x32_bf16 v[24:27], v[164:167], v[196:199], v[24:27]
	v_mfma_f32_16x16x32_bf16 v[20:23], v[172:175], v[196:199], v[20:23]
	v_mfma_f32_16x16x32_bf16 v[8:11], v[164:167], v[204:207], v[8:11]
	v_mfma_f32_16x16x32_bf16 v[4:7], v[172:175], v[204:207], v[4:7]
	s_setprio 0
	s_barrier
	s_add_i32 s89, 0, 0x18000
	v_add_u32_e32 v2, s89, v1
	s_add_i32 s90, 0, 0x1c000
	ds_read_b128 v[144:147], v2
	ds_read_b128 v[148:151], v2 offset:1024
	ds_read_b128 v[152:155], v2 offset:2048
	ds_read_b128 v[156:159], v2 offset:3072
	v_add_u32_e32 v2, s90, v1
	ds_read_b128 v[160:163], v2
	ds_read_b128 v[164:167], v2 offset:1024
	ds_read_b128 v[168:171], v2 offset:2048
	ds_read_b128 v[172:175], v2 offset:3072
	s_add_u32 s42, s42, 0x80000
	s_addc_u32 s43, s43, 0
	s_mov_b32 m0, s51
	ds_read_b128 v[176:179], v219 offset:32768
	ds_read_b128 v[180:183], v219 offset:33792
	ds_read_b128 v[184:187], v219 offset:34816
	ds_read_b128 v[188:191], v219 offset:35840
	ds_read_b128 v[192:195], v219 offset:36864
	ds_read_b128 v[196:199], v219 offset:37888
	ds_read_b128 v[200:203], v219 offset:38912
	ds_read_b128 v[204:207], v219 offset:39936
	global_load_lds_dwordx4 v138, s[42:43]
	s_mov_b32 m0, s60
	s_nop 0
	global_load_lds_dwordx4 v134, s[42:43]
	s_waitcnt vmcnt(8)
	s_waitcnt lgkmcnt(0)
	s_barrier
	s_setprio 1
	s_waitcnt lgkmcnt(0)
	v_mfma_f32_16x16x32_bf16 v[128:131], v[144:147], v[176:179], v[128:131]
	v_mfma_f32_16x16x32_bf16 v[124:127], v[152:155], v[176:179], v[124:127]
	v_mfma_f32_16x16x32_bf16 v[112:115], v[144:147], v[184:187], v[112:115]
	v_mfma_f32_16x16x32_bf16 v[108:111], v[152:155], v[184:187], v[108:111]
	v_mfma_f32_16x16x32_bf16 v[96:99], v[144:147], v[192:195], v[96:99]
	v_mfma_f32_16x16x32_bf16 v[92:95], v[152:155], v[192:195], v[92:95]
	v_mfma_f32_16x16x32_bf16 v[80:83], v[144:147], v[200:203], v[80:83]
	v_mfma_f32_16x16x32_bf16 v[76:79], v[152:155], v[200:203], v[76:79]
	v_mfma_f32_16x16x32_bf16 v[128:131], v[148:151], v[180:183], v[128:131]
	v_mfma_f32_16x16x32_bf16 v[124:127], v[156:159], v[180:183], v[124:127]
	v_mfma_f32_16x16x32_bf16 v[112:115], v[148:151], v[188:191], v[112:115]
	v_mfma_f32_16x16x32_bf16 v[108:111], v[156:159], v[188:191], v[108:111]
	v_mfma_f32_16x16x32_bf16 v[96:99], v[148:151], v[196:199], v[96:99]
	v_mfma_f32_16x16x32_bf16 v[92:95], v[156:159], v[196:199], v[92:95]
	v_mfma_f32_16x16x32_bf16 v[80:83], v[148:151], v[204:207], v[80:83]
	v_mfma_f32_16x16x32_bf16 v[76:79], v[156:159], v[204:207], v[76:79]
	s_setprio 0
	s_setprio 1
	v_mfma_f32_16x16x32_bf16 v[120:123], v[160:163], v[176:179], v[120:123]
	v_mfma_f32_16x16x32_bf16 v[116:119], v[168:171], v[176:179], v[116:119]
	v_mfma_f32_16x16x32_bf16 v[104:107], v[160:163], v[184:187], v[104:107]
	v_mfma_f32_16x16x32_bf16 v[100:103], v[168:171], v[184:187], v[100:103]
	v_mfma_f32_16x16x32_bf16 v[88:91], v[160:163], v[192:195], v[88:91]
	v_mfma_f32_16x16x32_bf16 v[84:87], v[168:171], v[192:195], v[84:87]
	v_mfma_f32_16x16x32_bf16 v[72:75], v[160:163], v[200:203], v[72:75]
	v_mfma_f32_16x16x32_bf16 v[68:71], v[168:171], v[200:203], v[68:71]
	v_mfma_f32_16x16x32_bf16 v[120:123], v[164:167], v[180:183], v[120:123]
	v_mfma_f32_16x16x32_bf16 v[116:119], v[172:175], v[180:183], v[116:119]
	v_mfma_f32_16x16x32_bf16 v[104:107], v[164:167], v[188:191], v[104:107]
	v_mfma_f32_16x16x32_bf16 v[100:103], v[172:175], v[188:191], v[100:103]
	v_mfma_f32_16x16x32_bf16 v[88:91], v[164:167], v[196:199], v[88:91]
	v_mfma_f32_16x16x32_bf16 v[84:87], v[172:175], v[196:199], v[84:87]
	v_mfma_f32_16x16x32_bf16 v[72:75], v[164:167], v[204:207], v[72:75]
	v_mfma_f32_16x16x32_bf16 v[68:71], v[172:175], v[204:207], v[68:71]
	s_setprio 0
	s_barrier
	s_add_i32 s42, s89, s45
	s_mov_b32 m0, s42
	ds_read_b128 v[176:179], v219 offset:49152
	ds_read_b128 v[180:183], v219 offset:50176
	ds_read_b128 v[184:187], v219 offset:51200
	ds_read_b128 v[188:191], v219 offset:52224
	ds_read_b128 v[192:195], v219 offset:53248
	ds_read_b128 v[196:199], v219 offset:54272
	ds_read_b128 v[200:203], v219 offset:55296
	ds_read_b128 v[204:207], v219 offset:56320
	global_load_lds_dwordx4 v136, s[98:99]
	s_add_i32 m0, s42, 0x2000
	s_add_u32 s40, s40, 0x80080
	s_addc_u32 s41, s41, 0
	s_add_i32 s42, s90, s45
	global_load_lds_dwordx4 v132, s[98:99]
	s_mov_b32 m0, s42
	s_nop 0
	global_load_lds_dwordx4 v136, s[40:41]
	s_add_i32 m0, s42, 0x2000
	s_nop 0
	global_load_lds_dwordx4 v132, s[40:41]
	s_mov_b32 m0, s61
	s_nop 0
	global_load_lds_dwordx4 v138, vcc
	s_mov_b32 m0, s80
	s_nop 0
	global_load_lds_dwordx4 v134, vcc
	s_waitcnt vmcnt(8)
	s_waitcnt lgkmcnt(0)
	s_barrier
	s_setprio 1
	s_waitcnt lgkmcnt(0)
	v_mfma_f32_16x16x32_bf16 v[64:67], v[144:147], v[176:179], v[64:67]
	v_mfma_f32_16x16x32_bf16 v[60:63], v[152:155], v[176:179], v[60:63]
	v_mfma_f32_16x16x32_bf16 v[48:51], v[144:147], v[184:187], v[48:51]
	v_mfma_f32_16x16x32_bf16 v[44:47], v[152:155], v[184:187], v[44:47]
	v_mfma_f32_16x16x32_bf16 v[32:35], v[144:147], v[192:195], v[32:35]
	v_mfma_f32_16x16x32_bf16 v[28:31], v[152:155], v[192:195], v[28:31]
	v_mfma_f32_16x16x32_bf16 v[16:19], v[144:147], v[200:203], v[16:19]
	v_mfma_f32_16x16x32_bf16 v[12:15], v[152:155], v[200:203], v[12:15]
	v_mfma_f32_16x16x32_bf16 v[64:67], v[148:151], v[180:183], v[64:67]
	v_mfma_f32_16x16x32_bf16 v[60:63], v[156:159], v[180:183], v[60:63]
	v_mfma_f32_16x16x32_bf16 v[48:51], v[148:151], v[188:191], v[48:51]
	v_mfma_f32_16x16x32_bf16 v[44:47], v[156:159], v[188:191], v[44:47]
	v_mfma_f32_16x16x32_bf16 v[32:35], v[148:151], v[196:199], v[32:35]
	v_mfma_f32_16x16x32_bf16 v[28:31], v[156:159], v[196:199], v[28:31]
	v_mfma_f32_16x16x32_bf16 v[16:19], v[148:151], v[204:207], v[16:19]
	v_mfma_f32_16x16x32_bf16 v[12:15], v[156:159], v[204:207], v[12:15]
	s_setprio 0
	s_setprio 1
	v_mfma_f32_16x16x32_bf16 v[56:59], v[160:163], v[176:179], v[56:59]
	v_mfma_f32_16x16x32_bf16 v[52:55], v[168:171], v[176:179], v[52:55]
	v_mfma_f32_16x16x32_bf16 v[40:43], v[160:163], v[184:187], v[40:43]
	v_mfma_f32_16x16x32_bf16 v[36:39], v[168:171], v[184:187], v[36:39]
	v_mfma_f32_16x16x32_bf16 v[24:27], v[160:163], v[192:195], v[24:27]
	v_mfma_f32_16x16x32_bf16 v[20:23], v[168:171], v[192:195], v[20:23]
	v_mfma_f32_16x16x32_bf16 v[8:11], v[160:163], v[200:203], v[8:11]
	v_mfma_f32_16x16x32_bf16 v[4:7], v[168:171], v[200:203], v[4:7]
	v_mfma_f32_16x16x32_bf16 v[56:59], v[164:167], v[180:183], v[56:59]
	v_mfma_f32_16x16x32_bf16 v[52:55], v[172:175], v[180:183], v[52:55]
	v_mfma_f32_16x16x32_bf16 v[40:43], v[164:167], v[188:191], v[40:43]
	v_mfma_f32_16x16x32_bf16 v[36:39], v[172:175], v[188:191], v[36:39]
	v_mfma_f32_16x16x32_bf16 v[24:27], v[164:167], v[196:199], v[24:27]
	v_mfma_f32_16x16x32_bf16 v[20:23], v[172:175], v[196:199], v[20:23]
	v_mfma_f32_16x16x32_bf16 v[8:11], v[164:167], v[204:207], v[8:11]
	v_mfma_f32_16x16x32_bf16 v[4:7], v[172:175], v[204:207], v[4:7]
	s_setprio 0
	s_barrier
	s_add_i32 s88, s88, 2
	s_add_u32 s38, s38, 0x100
	s_addc_u32 s39, s39, 0
	s_add_u32 s86, s86, 0x100
	s_addc_u32 s87, s87, 0
	s_cmp_gt_u32 s88, 29
	s_cbranch_scc0 .LBB0_732
	s_and_b64 vcc, exec, s[4:5]
	v_readlane_b32 s84, v239, 39
	s_mov_b32 s85, 0xf800000
	s_cbranch_vccz .LBB0_735
	s_barrier

.LBB0_805:
	s_add_u32 s40, s38, 0xfff80080
	s_addc_u32 s41, s39, -1
	s_add_i32 s89, 0, 0x10000
	s_cmp_eq_u32 s88, 28
	s_cselect_b32 s43, s9, s41
	s_cselect_b32 s42, s84, s40
	s_cselect_b32 s41, s11, s87
	s_cselect_b32 s40, s85, s86
	s_add_i32 s92, 0, 0x14000
	v_add_u32_e32 v158, s89, v144
	v_add_u32_e32 v174, s92, v144
	ds_read_b128 v[146:149], v158
	ds_read_b128 v[150:153], v158 offset:1024
	ds_read_b128 v[154:157], v158 offset:2048
	ds_read_b128 v[158:161], v158 offset:3072
	ds_read_b128 v[162:165], v174
	ds_read_b128 v[166:169], v174 offset:1024
	ds_read_b128 v[170:173], v174 offset:2048
	ds_read_b128 v[174:177], v174 offset:3072
	s_add_i32 m0, s48, 0xc000
	ds_read_b128 v[178:181], v145
	ds_read_b128 v[182:185], v145 offset:1024
	ds_read_b128 v[186:189], v145 offset:2048
	ds_read_b128 v[190:193], v145 offset:3072
	ds_read_b128 v[194:197], v145 offset:4096
	ds_read_b128 v[198:201], v145 offset:5120
	ds_read_b128 v[202:205], v145 offset:6144
	ds_read_b128 v[218:221], v145 offset:7168
	global_load_lds_dwordx4 v140, s[38:39]
	s_add_i32 m0, s48, 0xe000
	s_nop 0
	global_load_lds_dwordx4 v142, s[38:39]
	s_waitcnt vmcnt(8)
	s_waitcnt lgkmcnt(0)
	s_barrier
	s_setprio 1
	s_waitcnt lgkmcnt(0)
	v_mfma_f32_16x16x32_bf16 v[128:131], v[146:149], v[178:181], v[128:131]
	v_mfma_f32_16x16x32_bf16 v[124:127], v[154:157], v[178:181], v[124:127]
	v_mfma_f32_16x16x32_bf16 v[120:123], v[146:149], v[186:189], v[120:123]
	v_mfma_f32_16x16x32_bf16 v[116:119], v[154:157], v[186:189], v[116:119]
	v_mfma_f32_16x16x32_bf16 v[104:107], v[146:149], v[194:197], v[104:107]
	v_mfma_f32_16x16x32_bf16 v[100:103], v[154:157], v[194:197], v[100:103]
	v_mfma_f32_16x16x32_bf16 v[88:91], v[146:149], v[202:205], v[88:91]
	v_mfma_f32_16x16x32_bf16 v[84:87], v[154:157], v[202:205], v[84:87]
	v_mfma_f32_16x16x32_bf16 v[128:131], v[150:153], v[182:185], v[128:131]
	v_mfma_f32_16x16x32_bf16 v[124:127], v[158:161], v[182:185], v[124:127]
	v_mfma_f32_16x16x32_bf16 v[120:123], v[150:153], v[190:193], v[120:123]
	v_mfma_f32_16x16x32_bf16 v[116:119], v[158:161], v[190:193], v[116:119]
	v_mfma_f32_16x16x32_bf16 v[104:107], v[150:153], v[198:201], v[104:107]
	v_mfma_f32_16x16x32_bf16 v[100:103], v[158:161], v[198:201], v[100:103]
	v_mfma_f32_16x16x32_bf16 v[88:91], v[150:153], v[218:221], v[88:91]
	v_mfma_f32_16x16x32_bf16 v[84:87], v[158:161], v[218:221], v[84:87]
	s_setprio 0
	s_setprio 1
	v_mfma_f32_16x16x32_bf16 v[112:115], v[162:165], v[178:181], v[112:115]
	v_mfma_f32_16x16x32_bf16 v[108:111], v[170:173], v[178:181], v[108:111]
	v_mfma_f32_16x16x32_bf16 v[96:99], v[162:165], v[186:189], v[96:99]
	v_mfma_f32_16x16x32_bf16 v[92:95], v[170:173], v[186:189], v[92:95]
	v_mfma_f32_16x16x32_bf16 v[80:83], v[162:165], v[194:197], v[80:83]
	v_mfma_f32_16x16x32_bf16 v[76:79], v[170:173], v[194:197], v[76:79]
	v_mfma_f32_16x16x32_bf16 v[72:75], v[162:165], v[202:205], v[72:75]
	v_mfma_f32_16x16x32_bf16 v[68:71], v[170:173], v[202:205], v[68:71]
	v_mfma_f32_16x16x32_bf16 v[112:115], v[166:169], v[182:185], v[112:115]
	v_mfma_f32_16x16x32_bf16 v[108:111], v[174:177], v[182:185], v[108:111]
	v_mfma_f32_16x16x32_bf16 v[96:99], v[166:169], v[190:193], v[96:99]
	v_mfma_f32_16x16x32_bf16 v[92:95], v[174:177], v[190:193], v[92:95]
	v_mfma_f32_16x16x32_bf16 v[80:83], v[166:169], v[198:201], v[80:83]
	v_mfma_f32_16x16x32_bf16 v[76:79], v[174:177], v[198:201], v[76:79]
	v_mfma_f32_16x16x32_bf16 v[72:75], v[166:169], v[218:221], v[72:75]
	v_mfma_f32_16x16x32_bf16 v[68:71], v[174:177], v[218:221], v[68:71]
	s_setprio 0
	s_barrier
	s_add_i32 s89, s89, s45
	s_mov_b32 m0, s89
	ds_read_b128 v[178:181], v145 offset:16384
	ds_read_b128 v[182:185], v145 offset:17408
	ds_read_b128 v[186:189], v145 offset:18432
	ds_read_b128 v[190:193], v145 offset:19456
	ds_read_b128 v[194:197], v145 offset:20480
	ds_read_b128 v[198:201], v145 offset:21504
	ds_read_b128 v[202:205], v145 offset:22528
	ds_read_b128 v[218:221], v145 offset:23552
	global_load_lds_dwordx4 v2, s[40:41]
	s_add_i32 m0, s89, 0x2000
	s_add_u32 s90, s40, 0x80000
	s_addc_u32 s91, s41, 0
	s_add_i32 s89, s92, s45
	global_load_lds_dwordx4 v132, s[40:41]
	s_mov_b32 m0, s89
	s_nop 0
	global_load_lds_dwordx4 v2, s[90:91]
	s_add_i32 m0, s89, 0x2000
	s_nop 0
	global_load_lds_dwordx4 v132, s[90:91]
	s_mov_b32 m0, s48
	s_nop 0
	global_load_lds_dwordx4 v136, s[42:43]
	s_mov_b32 m0, s49
	s_nop 0
	global_load_lds_dwordx4 v134, s[42:43]
	s_add_u32 s98, s40, s16
	s_addc_u32 s99, s41, s17
	s_add_u32 vcc_lo, s42, s16
	s_addc_u32 vcc_hi, s43, s17
	s_waitcnt vmcnt(8)
	s_waitcnt lgkmcnt(0)
	s_barrier
	s_setprio 1
	s_waitcnt lgkmcnt(0)
	v_mfma_f32_16x16x32_bf16 v[64:67], v[146:149], v[178:181], v[64:67]
	v_mfma_f32_16x16x32_bf16 v[60:63], v[154:157], v[178:181], v[60:63]
	v_mfma_f32_16x16x32_bf16 v[56:59], v[146:149], v[186:189], v[56:59]
	v_mfma_f32_16x16x32_bf16 v[52:55], v[154:157], v[186:189], v[52:55]
	v_mfma_f32_16x16x32_bf16 v[40:43], v[146:149], v[194:197], v[40:43]
	v_mfma_f32_16x16x32_bf16 v[36:39], v[154:157], v[194:197], v[36:39]
	v_mfma_f32_16x16x32_bf16 v[24:27], v[146:149], v[202:205], v[24:27]
	v_mfma_f32_16x16x32_bf16 v[20:23], v[154:157], v[202:205], v[20:23]
	v_mfma_f32_16x16x32_bf16 v[64:67], v[150:153], v[182:185], v[64:67]
	v_mfma_f32_16x16x32_bf16 v[60:63], v[158:161], v[182:185], v[60:63]
	v_mfma_f32_16x16x32_bf16 v[56:59], v[150:153], v[190:193], v[56:59]
	v_mfma_f32_16x16x32_bf16 v[52:55], v[158:161], v[190:193], v[52:55]
	v_mfma_f32_16x16x32_bf16 v[40:43], v[150:153], v[198:201], v[40:43]
	v_mfma_f32_16x16x32_bf16 v[36:39], v[158:161], v[198:201], v[36:39]
	v_mfma_f32_16x16x32_bf16 v[24:27], v[150:153], v[218:221], v[24:27]
	v_mfma_f32_16x16x32_bf16 v[20:23], v[158:161], v[218:221], v[20:23]
	s_setprio 0
	s_setprio 1
	v_mfma_f32_16x16x32_bf16 v[48:51], v[162:165], v[178:181], v[48:51]
	v_mfma_f32_16x16x32_bf16 v[44:47], v[170:173], v[178:181], v[44:47]
	v_mfma_f32_16x16x32_bf16 v[32:35], v[162:165], v[186:189], v[32:35]
	v_mfma_f32_16x16x32_bf16 v[28:31], v[170:173], v[186:189], v[28:31]
	v_mfma_f32_16x16x32_bf16 v[16:19], v[162:165], v[194:197], v[16:19]
	v_mfma_f32_16x16x32_bf16 v[12:15], v[170:173], v[194:197], v[12:15]
	v_mfma_f32_16x16x32_bf16 v[8:11], v[162:165], v[202:205], v[8:11]
	v_mfma_f32_16x16x32_bf16 v[4:7], v[170:173], v[202:205], v[4:7]
	v_mfma_f32_16x16x32_bf16 v[48:51], v[166:169], v[182:185], v[48:51]
	v_mfma_f32_16x16x32_bf16 v[44:47], v[174:177], v[182:185], v[44:47]
	v_mfma_f32_16x16x32_bf16 v[32:35], v[166:169], v[190:193], v[32:35]
	v_mfma_f32_16x16x32_bf16 v[28:31], v[174:177], v[190:193], v[28:31]
	v_mfma_f32_16x16x32_bf16 v[16:19], v[166:169], v[198:201], v[16:19]
	v_mfma_f32_16x16x32_bf16 v[12:15], v[174:177], v[198:201], v[12:15]
	v_mfma_f32_16x16x32_bf16 v[8:11], v[166:169], v[218:221], v[8:11]
	v_mfma_f32_16x16x32_bf16 v[4:7], v[174:177], v[218:221], v[4:7]
	s_setprio 0
	s_barrier
	s_add_i32 s89, 0, 0x18000
	s_add_i32 s90, 0, 0x1c000
	v_add_u32_e32 v158, s89, v144
	v_add_u32_e32 v174, s90, v144
	ds_read_b128 v[146:149], v158
	ds_read_b128 v[150:153], v158 offset:1024
	ds_read_b128 v[154:157], v158 offset:2048
	ds_read_b128 v[158:161], v158 offset:3072
	ds_read_b128 v[162:165], v174
	ds_read_b128 v[166:169], v174 offset:1024
	ds_read_b128 v[170:173], v174 offset:2048
	ds_read_b128 v[174:177], v174 offset:3072
	s_add_u32 s42, s42, 0x80000
	s_addc_u32 s43, s43, 0
	s_mov_b32 m0, s51
	ds_read_b128 v[178:181], v145 offset:32768
	ds_read_b128 v[182:185], v145 offset:33792
	ds_read_b128 v[186:189], v145 offset:34816
	ds_read_b128 v[190:193], v145 offset:35840
	ds_read_b128 v[194:197], v145 offset:36864
	ds_read_b128 v[198:201], v145 offset:37888
	ds_read_b128 v[202:205], v145 offset:38912
	ds_read_b128 v[218:221], v145 offset:39936
	global_load_lds_dwordx4 v136, s[42:43]
	s_mov_b32 m0, s60
	s_nop 0
	global_load_lds_dwordx4 v134, s[42:43]
	s_waitcnt vmcnt(8)
	s_waitcnt lgkmcnt(0)
	s_barrier
	s_setprio 1
	s_waitcnt lgkmcnt(0)
	v_mfma_f32_16x16x32_bf16 v[128:131], v[146:149], v[178:181], v[128:131]
	v_mfma_f32_16x16x32_bf16 v[124:127], v[154:157], v[178:181], v[124:127]
	v_mfma_f32_16x16x32_bf16 v[120:123], v[146:149], v[186:189], v[120:123]
	v_mfma_f32_16x16x32_bf16 v[116:119], v[154:157], v[186:189], v[116:119]
	v_mfma_f32_16x16x32_bf16 v[104:107], v[146:149], v[194:197], v[104:107]
	v_mfma_f32_16x16x32_bf16 v[100:103], v[154:157], v[194:197], v[100:103]
	v_mfma_f32_16x16x32_bf16 v[88:91], v[146:149], v[202:205], v[88:91]
	v_mfma_f32_16x16x32_bf16 v[84:87], v[154:157], v[202:205], v[84:87]
	v_mfma_f32_16x16x32_bf16 v[128:131], v[150:153], v[182:185], v[128:131]
	v_mfma_f32_16x16x32_bf16 v[124:127], v[158:161], v[182:185], v[124:127]
	v_mfma_f32_16x16x32_bf16 v[120:123], v[150:153], v[190:193], v[120:123]
	v_mfma_f32_16x16x32_bf16 v[116:119], v[158:161], v[190:193], v[116:119]
	v_mfma_f32_16x16x32_bf16 v[104:107], v[150:153], v[198:201], v[104:107]
	v_mfma_f32_16x16x32_bf16 v[100:103], v[158:161], v[198:201], v[100:103]
	v_mfma_f32_16x16x32_bf16 v[88:91], v[150:153], v[218:221], v[88:91]
	v_mfma_f32_16x16x32_bf16 v[84:87], v[158:161], v[218:221], v[84:87]
	s_setprio 0
	s_setprio 1
	v_mfma_f32_16x16x32_bf16 v[112:115], v[162:165], v[178:181], v[112:115]
	v_mfma_f32_16x16x32_bf16 v[108:111], v[170:173], v[178:181], v[108:111]
	v_mfma_f32_16x16x32_bf16 v[96:99], v[162:165], v[186:189], v[96:99]
	v_mfma_f32_16x16x32_bf16 v[92:95], v[170:173], v[186:189], v[92:95]
	v_mfma_f32_16x16x32_bf16 v[80:83], v[162:165], v[194:197], v[80:83]
	v_mfma_f32_16x16x32_bf16 v[76:79], v[170:173], v[194:197], v[76:79]
	v_mfma_f32_16x16x32_bf16 v[72:75], v[162:165], v[202:205], v[72:75]
	v_mfma_f32_16x16x32_bf16 v[68:71], v[170:173], v[202:205], v[68:71]
	v_mfma_f32_16x16x32_bf16 v[112:115], v[166:169], v[182:185], v[112:115]
	v_mfma_f32_16x16x32_bf16 v[108:111], v[174:177], v[182:185], v[108:111]
	v_mfma_f32_16x16x32_bf16 v[96:99], v[166:169], v[190:193], v[96:99]
	v_mfma_f32_16x16x32_bf16 v[92:95], v[174:177], v[190:193], v[92:95]
	v_mfma_f32_16x16x32_bf16 v[80:83], v[166:169], v[198:201], v[80:83]
	v_mfma_f32_16x16x32_bf16 v[76:79], v[174:177], v[198:201], v[76:79]
	v_mfma_f32_16x16x32_bf16 v[72:75], v[166:169], v[218:221], v[72:75]
	v_mfma_f32_16x16x32_bf16 v[68:71], v[174:177], v[218:221], v[68:71]
	s_setprio 0
	s_barrier
	s_add_i32 s42, s89, s45
	s_mov_b32 m0, s42
	ds_read_b128 v[178:181], v145 offset:49152
	ds_read_b128 v[182:185], v145 offset:50176
	ds_read_b128 v[186:189], v145 offset:51200
	ds_read_b128 v[190:193], v145 offset:52224
	ds_read_b128 v[194:197], v145 offset:53248
	ds_read_b128 v[198:201], v145 offset:54272
	ds_read_b128 v[202:205], v145 offset:55296
	ds_read_b128 v[218:221], v145 offset:56320
	global_load_lds_dwordx4 v2, s[98:99]
	s_add_i32 m0, s42, 0x2000
	s_add_u32 s40, s40, 0x80080
	s_addc_u32 s41, s41, 0
	s_add_i32 s42, s90, s45
	global_load_lds_dwordx4 v132, s[98:99]
	s_mov_b32 m0, s42
	s_nop 0
	global_load_lds_dwordx4 v2, s[40:41]
	s_add_i32 m0, s42, 0x2000
	s_nop 0
	global_load_lds_dwordx4 v132, s[40:41]
	s_mov_b32 m0, s61
	s_nop 0
	global_load_lds_dwordx4 v136, vcc
	s_mov_b32 m0, s80
	s_nop 0
	global_load_lds_dwordx4 v134, vcc
	s_waitcnt vmcnt(8)
	s_waitcnt lgkmcnt(0)
	s_barrier
	s_setprio 1
	s_waitcnt lgkmcnt(0)
	v_mfma_f32_16x16x32_bf16 v[64:67], v[146:149], v[178:181], v[64:67]
	v_mfma_f32_16x16x32_bf16 v[60:63], v[154:157], v[178:181], v[60:63]
	v_mfma_f32_16x16x32_bf16 v[56:59], v[146:149], v[186:189], v[56:59]
	v_mfma_f32_16x16x32_bf16 v[52:55], v[154:157], v[186:189], v[52:55]
	v_mfma_f32_16x16x32_bf16 v[40:43], v[146:149], v[194:197], v[40:43]
	v_mfma_f32_16x16x32_bf16 v[36:39], v[154:157], v[194:197], v[36:39]
	v_mfma_f32_16x16x32_bf16 v[24:27], v[146:149], v[202:205], v[24:27]
	v_mfma_f32_16x16x32_bf16 v[20:23], v[154:157], v[202:205], v[20:23]
	v_mfma_f32_16x16x32_bf16 v[64:67], v[150:153], v[182:185], v[64:67]
	v_mfma_f32_16x16x32_bf16 v[60:63], v[158:161], v[182:185], v[60:63]
	v_mfma_f32_16x16x32_bf16 v[56:59], v[150:153], v[190:193], v[56:59]
	v_mfma_f32_16x16x32_bf16 v[52:55], v[158:161], v[190:193], v[52:55]
	v_mfma_f32_16x16x32_bf16 v[40:43], v[150:153], v[198:201], v[40:43]
	v_mfma_f32_16x16x32_bf16 v[36:39], v[158:161], v[198:201], v[36:39]
	v_mfma_f32_16x16x32_bf16 v[24:27], v[150:153], v[218:221], v[24:27]
	v_mfma_f32_16x16x32_bf16 v[20:23], v[158:161], v[218:221], v[20:23]
	s_setprio 0
	s_setprio 1
	v_mfma_f32_16x16x32_bf16 v[48:51], v[162:165], v[178:181], v[48:51]
	v_mfma_f32_16x16x32_bf16 v[44:47], v[170:173], v[178:181], v[44:47]
	v_mfma_f32_16x16x32_bf16 v[32:35], v[162:165], v[186:189], v[32:35]
	v_mfma_f32_16x16x32_bf16 v[28:31], v[170:173], v[186:189], v[28:31]
	v_mfma_f32_16x16x32_bf16 v[16:19], v[162:165], v[194:197], v[16:19]
	v_mfma_f32_16x16x32_bf16 v[12:15], v[170:173], v[194:197], v[12:15]
	v_mfma_f32_16x16x32_bf16 v[8:11], v[162:165], v[202:205], v[8:11]
	v_mfma_f32_16x16x32_bf16 v[4:7], v[170:173], v[202:205], v[4:7]
	v_mfma_f32_16x16x32_bf16 v[48:51], v[166:169], v[182:185], v[48:51]
	v_mfma_f32_16x16x32_bf16 v[44:47], v[174:177], v[182:185], v[44:47]
	v_mfma_f32_16x16x32_bf16 v[32:35], v[166:169], v[190:193], v[32:35]
	v_mfma_f32_16x16x32_bf16 v[28:31], v[174:177], v[190:193], v[28:31]
	v_mfma_f32_16x16x32_bf16 v[16:19], v[166:169], v[198:201], v[16:19]
	v_mfma_f32_16x16x32_bf16 v[12:15], v[174:177], v[198:201], v[12:15]
	v_mfma_f32_16x16x32_bf16 v[8:11], v[166:169], v[218:221], v[8:11]
	v_mfma_f32_16x16x32_bf16 v[4:7], v[174:177], v[218:221], v[4:7]
	s_setprio 0
	s_barrier
	s_add_i32 s88, s88, 2
	s_add_u32 s38, s38, 0x100
	s_addc_u32 s39, s39, 0
	s_add_u32 s86, s86, 0x100
	s_addc_u32 s87, s87, 0
	s_cmp_gt_u32 s88, 29
	s_cbranch_scc0 .LBB0_805
	s_and_b64 vcc, exec, s[4:5]
	v_readlane_b32 s84, v239, 39
	s_mov_b32 s85, 0xf800000
	s_cbranch_vccz .LBB0_808
	s_barrier
